# baseline (speedup 1.0000x reference)
.LBB2_13:
	v_exp_f32_e32 v48, v48
	v_exp_f32_e32 v49, v49
	v_mfma_f32_32x32x16_bf16 v[112:127], a[192:195], a[128:131], v[16:31]
	ds_read_b64_tr_b16 v[180:181], v223 offset:0
	v_cvt_pk_bf16_f32 v164, v128, v129
	v_exp_f32_e32 v50, v50
	v_exp_f32_e32 v51, v51
	v_mfma_f32_32x32x16_bf16 v[96:111], a[192:195], a[160:163], v[0:15]
	ds_read_b64_tr_b16 v[182:183], v223 offset:0x800
	v_cvt_pk_bf16_f32 v165, v130, v131
	v_mfma_f32_32x32x16_bf16 v[80:95], a[224:227], a[128:131], v[16:31]
	ds_read_b64_tr_b16 v[184:185], v223 offset:0x200
	v_exp_f32_e32 v236, v52
	v_exp_f32_e32 v237, v53
	v_cvt_pk_bf16_f32 v166, v132, v133
	v_mfma_f32_32x32x16_bf16 v[64:79], a[224:227], a[160:163], v[0:15]
	ds_read_b64_tr_b16 v[186:187], v223 offset:0xa00
	ds_read_b64_tr_b16 v[176:177], v223 offset:0x400
	v_exp_f32_e32 v242, v54
	v_exp_f32_e32 v243, v55
	v_cvt_pk_bf16_f32 v167, v134, v135
	v_exp_f32_e32 v198, v56
	v_exp_f32_e32 v199, v57
	v_mfma_f32_32x32x16_bf16 v[112:127], a[196:199], a[132:135], v[112:127]
	ds_read_b64_tr_b16 v[178:179], v223 offset:0xc00
	v_cvt_pk_bf16_f32 v128, v136, v137
	v_exp_f32_e32 v230, v58
	v_exp_f32_e32 v231, v59
	v_mfma_f32_32x32x16_bf16 v[96:111], a[196:199], a[164:167], v[96:111]
	ds_read_b64_tr_b16 v[188:189], v223 offset:0x600
	v_cvt_pk_bf16_f32 v129, v138, v139
	v_exp_f32_e32 v232, v60
	v_exp_f32_e32 v233, v61
	v_mfma_f32_32x32x16_bf16 v[80:95], a[228:231], a[132:135], v[80:95]
	ds_read_b64_tr_b16 v[190:191], v223 offset:0xe00
	v_cvt_pk_bf16_f32 v130, v140, v141
	v_mfma_f32_32x32x16_bf16 v[64:79], a[228:231], a[164:167], v[64:79]
	ds_read_b64_tr_b16 v[172:173], v223 offset:0x1000
	v_exp_f32_e32 v234, v62
	v_exp_f32_e32 v235, v63
	ds_read_b64_tr_b16 v[174:175], v223 offset:0x1800
	v_cvt_pk_bf16_f32 v131, v142, v143
	v_exp_f32_e32 v141, v32
	v_exp_f32_e32 v142, v33
	v_mfma_f32_32x32x16_bf16 v[112:127], a[200:203], a[136:139], v[112:127]
	ds_read_b64_tr_b16 v[168:169], v223 offset:0x1200
	v_cvt_pk_bf16_f32 v192, v144, v145
	v_exp_f32_e32 v143, v34
	v_mfma_f32_32x32x16_bf16 v[96:111], a[200:203], a[168:171], v[96:111]
	ds_read_b64_tr_b16 v[170:171], v223 offset:0x1a00
	v_exp_f32_e32 v244, v35
	v_cvt_pk_bf16_f32 v193, v146, v147
	v_mfma_f32_32x32x16_bf16 v[80:95], a[232:235], a[136:139], v[80:95]
	ds_read_b64_tr_b16 v[160:161], v223 offset:0x1400
	v_exp_f32_e32 v245, v36
	v_exp_f32_e32 v246, v37
	v_cvt_pk_bf16_f32 v194, v148, v149
	v_mfma_f32_32x32x16_bf16 v[64:79], a[232:235], a[168:171], v[64:79]
	ds_read_b64_tr_b16 v[162:163], v223 offset:0x1c00
	ds_read_b64_tr_b16 v[136:137], v223 offset:0x1600
	v_exp_f32_e32 v247, v38
	v_exp_f32_e32 v248, v39
	v_cvt_pk_bf16_f32 v195, v150, v151
	v_exp_f32_e32 v148, v40
	v_exp_f32_e32 v149, v41
	v_mfma_f32_32x32x16_bf16 v[112:127], a[204:207], a[140:143], v[112:127]
	ds_read_b64_tr_b16 v[138:139], v223 offset:0x1e00
	v_cvt_pk_bf16_f32 v144, v152, v153
	v_exp_f32_e32 v150, v42
	v_exp_f32_e32 v151, v43
	v_mfma_f32_32x32x16_bf16 v[96:111], a[204:207], a[172:175], v[96:111]
	ds_read_b64_tr_b16 v[132:133], v223 offset:0x2000
	v_cvt_pk_bf16_f32 v145, v154, v155
	v_exp_f32_e32 v152, v44
	v_exp_f32_e32 v153, v45
	v_mfma_f32_32x32x16_bf16 v[80:95], a[236:239], a[140:143], v[80:95]
	ds_read_b64_tr_b16 v[134:135], v223 offset:0x2800
	v_cvt_pk_bf16_f32 v146, v156, v157
	v_mfma_f32_32x32x16_bf16 v[64:79], a[236:239], a[172:175], v[64:79]
	ds_read_b64_tr_b16 v[60:61], v223 offset:0x2200
	v_exp_f32_e32 v154, v46
	v_exp_f32_e32 v155, v47
	ds_read_b64_tr_b16 v[62:63], v223 offset:0x2a00
	v_cvt_pk_bf16_f32 v147, v158, v159
	v_mfma_f32_32x32x16_bf16 v[112:127], a[208:211], a[144:147], v[112:127]
	ds_read_b64_tr_b16 v[56:57], v223 offset:0x2400
	v_cvt_pk_bf16_f32 v52, v48, v49
	v_add_f32_e32 v32, v239, v48
	v_add_f32_e32 v33, v238, v49
	s_add_i32 s19, s17, 0xfffda000
	v_mfma_f32_32x32x16_bf16 v[96:111], a[208:211], a[176:179], v[96:111]
	ds_read_b64_tr_b16 v[58:59], v223 offset:0x2c00
	v_cvt_pk_bf16_f32 v53, v50, v51
	v_add_f32_e32 v32, v32, v50
	v_add_f32_e32 v33, v33, v51
	v_mfma_f32_32x32x16_bf16 v[80:95], a[240:243], a[144:147], v[80:95]
	ds_read_b64_tr_b16 v[48:49], v223 offset:0x2600
	v_cvt_pk_bf16_f32 v54, v236, v237
	v_add_f32_e32 v32, v32, v236
	v_add_f32_e32 v33, v33, v237
	s_add_i32 s82, s17, 0xfffdc000
	v_mfma_f32_32x32x16_bf16 v[64:79], a[240:243], a[176:179], v[64:79]
	ds_read_b64_tr_b16 v[50:51], v223 offset:0x2e00
	ds_read_b64_tr_b16 v[44:45], v223 offset:0x3000
	v_cvt_pk_bf16_f32 v55, v242, v243
	v_add_f32_e32 v32, v32, v242
	v_add_f32_e32 v33, v33, v243
	v_mfma_f32_32x32x16_bf16 v[112:127], a[212:215], a[148:151], v[112:127]
	ds_read_b64_tr_b16 v[46:47], v223 offset:0x3800
	v_add_f32_e32 v32, v32, v198
	v_add_f32_e32 v33, v33, v199
	s_add_i32 s24, s17, 0xfffde000
	v_mfma_f32_32x32x16_bf16 v[96:111], a[212:215], a[180:183], v[96:111]
	ds_read_b64_tr_b16 v[40:41], v223 offset:0x3200
	v_add_f32_e32 v32, v32, v230
	v_add_f32_e32 v33, v33, v231
	v_mfma_f32_32x32x16_bf16 v[80:95], a[244:247], a[148:151], v[80:95]
	ds_read_b64_tr_b16 v[42:43], v223 offset:0x3a00
	v_add_f32_e32 v32, v32, v232
	v_add_f32_e32 v33, v33, v233
	s_add_i32 s86, s17, 0xfffe0000
	v_mfma_f32_32x32x16_bf16 v[64:79], a[244:247], a[180:183], v[64:79]
	ds_read_b64_tr_b16 v[36:37], v223 offset:0x3400
	ds_read_b64_tr_b16 v[38:39], v223 offset:0x3c00
	v_add_f32_e32 v156, v32, v234
	v_add_f32_e32 v157, v33, v235
	v_mfma_f32_32x32x16_bf16 v[112:127], a[216:219], a[152:155], v[112:127]
	ds_read_b64_tr_b16 v[32:33], v223 offset:0x3600
	v_cvt_pk_bf16_f32 v140, v141, v142
	v_add_f32_e32 v158, v240, v141
	v_add_f32_e32 v142, v241, v142
	s_add_i32 s88, s17, 0xfffba000
	v_mfma_f32_32x32x16_bf16 v[96:111], a[216:219], a[184:187], v[96:111]
	ds_read_b64_tr_b16 v[34:35], v223 offset:0x3e00
	v_cvt_pk_bf16_f32 v141, v143, v244
	v_add_f32_e32 v143, v158, v143
	v_add_f32_e32 v158, v142, v244
	v_mfma_f32_32x32x16_bf16 v[80:95], a[248:251], a[152:155], v[80:95]
	v_cvt_pk_bf16_f32 v142, v245, v246
	v_add_f32_e32 v159, v143, v245
	v_add_f32_e32 v158, v158, v246
	v_mfma_f32_32x32x16_bf16 v[64:79], a[248:251], a[184:187], v[64:79]
	s_add_i32 s90, s17, 0xfffba080
	v_cvt_pk_bf16_f32 v143, v247, v248
	v_add_f32_e32 v159, v159, v247
	v_add_f32_e32 v158, v158, v248
	v_mfma_f32_32x32x16_bf16 v[112:127], a[220:223], a[156:159], v[112:127]
	v_add_f32_e32 v159, v159, v148
	v_add_f32_e32 v158, v158, v149
	v_mfma_f32_32x32x16_bf16 v[96:111], a[220:223], a[188:191], v[96:111]
	s_add_i32 s92, s17, 0xfffbe000
	v_add_f32_e32 v159, v159, v150
	v_add_f32_e32 v158, v158, v151
	v_mfma_f32_32x32x16_bf16 v[80:95], a[252:255], a[156:159], v[80:95]
	v_add_f32_e32 v159, v159, v152
	v_add_f32_e32 v158, v158, v153
	v_mfma_f32_32x32x16_bf16 v[64:79], a[252:255], a[188:191], v[64:79]
	s_add_i32 s94, s17, 0xfffbe080
	v_add_f32_e32 v159, v159, v154
	v_add_f32_e32 v158, v158, v155
	s_nop 4
	v_add_f32_e32 v156, v156, v157
	s_waitcnt vmcnt(0) lgkmcnt(0)
	s_barrier
	s_nop 0
	v_mov_b32_e32 v157, v156
	s_nop 1
	v_permlane32_swap_b32_e32 v156, v157
	v_add_f32_e32 v156, v156, v157
	v_add_f32_e32 v197, v197, v156
	v_add_f32_e32 v156, v159, v158
	v_mov_b32_e32 v157, v156
	s_nop 1
	v_permlane32_swap_b32_e32 v156, v157
	v_add_f32_e32 v156, v156, v157
	v_add_f32_e32 v196, v196, v156
	s_nop 1
	v_mfma_f32_32x32x16_bf16 a[0:15], v[180:183], v[164:167], a[0:15]
	s_mov_b32 m0, s30
	s_nop 0
	buffer_load_dwordx4 v209, s[4:7], s19 offen lds
	v_mfma_f32_32x32x16_bf16 a[16:31], v[180:183], v[192:195], a[16:31]
	s_mov_b32 m0, s37
	s_nop 0
	buffer_load_dwordx4 v210, s[4:7], s82 offen lds
	ds_read_b128 a[192:195], v219 offset:0
	v_mfma_f32_32x32x16_bf16 a[32:47], v[184:187], v[164:167], a[32:47]
	s_mov_b32 m0, s39
	s_nop 0
	buffer_load_dwordx4 v209, s[4:7], s24 offen lds
	ds_read_b128 a[196:199], v220 offset:0
	v_mfma_f32_32x32x16_bf16 a[48:63], v[184:187], v[192:195], a[48:63]
	s_mov_b32 m0, s41
	s_nop 0
	buffer_load_dwordx4 v210, s[4:7], s86 offen lds
	ds_read_b128 a[200:203], v221 offset:0
	v_mfma_f32_32x32x16_bf16 a[64:79], v[176:179], v[164:167], a[64:79]
	s_mov_b32 m0, s43
	s_nop 0
	buffer_load_dwordx4 v211, s[20:23], s88 offen lds
	ds_read_b128 a[204:207], v222 offset:0
	v_mfma_f32_32x32x16_bf16 a[80:95], v[176:179], v[192:195], a[80:95]
	s_mov_b32 m0, s45
	s_nop 0
	buffer_load_dwordx4 v211, s[20:23], s90 offen lds
	ds_read_b128 a[208:211], v219 offset:128
	v_mfma_f32_32x32x16_bf16 a[96:111], v[188:191], v[164:167], a[96:111]
	s_mov_b32 m0, s47
	s_nop 0
	buffer_load_dwordx4 v211, s[20:23], s92 offen lds
	ds_read_b128 a[212:215], v220 offset:128
	v_mfma_f32_32x32x16_bf16 a[112:127], v[188:191], v[192:195], a[112:127]
	s_mov_b32 m0, s49
	s_nop 0
	buffer_load_dwordx4 v211, s[20:23], s94 offen lds
	ds_read_b128 a[216:219], v221 offset:128
	v_mfma_f32_32x32x16_bf16 a[0:15], v[172:175], v[128:131], a[0:15]
	ds_read_b128 a[220:223], v222 offset:128
	v_max3_f32 v156, v112, v113, v80
	v_max3_f32 v157, v114, v115, v81
	v_max3_f32 v156, v156, v82, v83
	v_mfma_f32_32x32x16_bf16 a[16:31], v[172:175], v[144:147], a[16:31]
	ds_read_b128 a[224:227], v219 offset:8192
	v_max3_f32 v156, v156, v116, v117
	v_max3_f32 v157, v157, v118, v119
	v_max3_f32 v156, v156, v84, v85
	v_max3_f32 v157, v157, v86, v87
	v_mfma_f32_32x32x16_bf16 a[32:47], v[168:171], v[128:131], a[32:47]
	ds_read_b128 a[228:231], v220 offset:8192
	v_max3_f32 v156, v156, v120, v121
	v_max3_f32 v157, v157, v122, v123
	v_max3_f32 v156, v156, v88, v89
	v_max3_f32 v157, v157, v90, v91
	v_mfma_f32_32x32x16_bf16 a[48:63], v[168:171], v[144:147], a[48:63]
	ds_read_b128 a[232:235], v221 offset:8192
	v_max3_f32 v156, v156, v124, v125
	v_max3_f32 v157, v157, v126, v127
	v_max3_f32 v156, v156, v92, v93
	v_max3_f32 v157, v157, v94, v95
	v_mfma_f32_32x32x16_bf16 a[64:79], v[160:163], v[128:131], a[64:79]
	ds_read_b128 a[236:239], v222 offset:8192
	v_max3_f32 v158, v96, v97, v64
	v_max3_f32 v159, v98, v99, v65
	v_max3_f32 v158, v158, v66, v67
	v_mfma_f32_32x32x16_bf16 a[80:95], v[160:163], v[144:147], a[80:95]
	ds_read_b128 a[240:243], v219 offset:8320
	v_max3_f32 v158, v158, v100, v101
	v_max3_f32 v159, v159, v102, v103
	v_max3_f32 v158, v158, v68, v69
	v_max3_f32 v159, v159, v70, v71
	v_mfma_f32_32x32x16_bf16 a[96:111], v[136:139], v[128:131], a[96:111]
	ds_read_b128 a[244:247], v220 offset:8320
	v_max3_f32 v128, v158, v104, v105
	v_max3_f32 v129, v159, v106, v107
	v_max3_f32 v128, v128, v72, v73
	v_max3_f32 v129, v129, v74, v75
	v_mfma_f32_32x32x16_bf16 a[112:127], v[136:139], v[144:147], a[112:127]
	ds_read_b128 a[248:251], v221 offset:8320
	v_max3_f32 v128, v128, v108, v109
	v_max3_f32 v129, v129, v110, v111
	v_max3_f32 v128, v128, v76, v77
	v_max3_f32 v130, v129, v78, v79
	v_mfma_f32_32x32x16_bf16 a[0:15], v[132:135], v[52:55], a[0:15]
	ds_read_b128 a[252:255], v222 offset:8320
	v_max_f32_e32 v129, v156, v157
	v_mov_b32_e32 v131, v129
	s_nop 1
	v_permlane32_swap_b32_e32 v129, v131
	v_max_f32_e32 v129, v129, v131
	v_mfma_f32_32x32x16_bf16 a[16:31], v[132:135], v[140:143], a[16:31]
	v_max_f32_e32 v128, v128, v130
	v_mov_b32_e32 v130, v128
	s_nop 1
	v_permlane32_swap_b32_e32 v128, v130
	v_max_f32_e32 v128, v128, v130
	v_max_f32_e32 v130, v129, v129
	v_max_f32_e32 v131, v128, v128
	v_max_f32_e32 v130, v130, v131
	v_mfma_f32_32x32x16_bf16 a[32:47], v[60:63], v[52:55], a[32:47]
	v_cmp_lt_f32_e32 vcc, s79, v130
	s_cmp_lg_u64 vcc, 0
	s_cselect_b64 s[0:1], -1, 0
	s_cbranch_vccnz .LBB2_18

.LBB2_15:
	s_waitcnt lgkmcnt(0)
	v_exp_f32_e32 v80, v80
	v_exp_f32_e32 v81, v81
	v_mfma_f32_32x32x16_bf16 v[112:127], a[192:195], a[128:131], v[16:31]
	ds_read_b64_tr_b16 v[180:181], v208 offset:0
	v_cvt_pk_bf16_f32 v164, v128, v129
	v_exp_f32_e32 v82, v82
	v_exp_f32_e32 v83, v83
	v_mfma_f32_32x32x16_bf16 v[96:111], a[192:195], a[160:163], v[0:15]
	ds_read_b64_tr_b16 v[182:183], v208 offset:0x800
	v_cvt_pk_bf16_f32 v165, v130, v131
	v_mfma_f32_32x32x16_bf16 v[48:63], a[224:227], a[128:131], v[16:31]
	ds_read_b64_tr_b16 v[184:185], v208 offset:0x200
	v_exp_f32_e32 v240, v84
	v_exp_f32_e32 v241, v85
	v_cvt_pk_bf16_f32 v166, v132, v133
	v_mfma_f32_32x32x16_bf16 v[32:47], a[224:227], a[160:163], v[0:15]
	ds_read_b64_tr_b16 v[186:187], v208 offset:0xa00
	ds_read_b64_tr_b16 v[176:177], v208 offset:0x400
	v_exp_f32_e32 v242, v86
	v_exp_f32_e32 v243, v87
	v_cvt_pk_bf16_f32 v167, v134, v135
	v_exp_f32_e32 v198, v88
	v_exp_f32_e32 v199, v89
	v_mfma_f32_32x32x16_bf16 v[112:127], a[196:199], a[132:135], v[112:127]
	ds_read_b64_tr_b16 v[178:179], v208 offset:0xc00
	v_cvt_pk_bf16_f32 v128, v136, v137
	v_exp_f32_e32 v230, v90
	v_exp_f32_e32 v231, v91
	v_mfma_f32_32x32x16_bf16 v[96:111], a[196:199], a[164:167], v[96:111]
	ds_read_b64_tr_b16 v[188:189], v208 offset:0x600
	v_cvt_pk_bf16_f32 v129, v138, v139
	v_exp_f32_e32 v232, v92
	v_exp_f32_e32 v233, v93
	v_mfma_f32_32x32x16_bf16 v[48:63], a[228:231], a[132:135], v[48:63]
	ds_read_b64_tr_b16 v[190:191], v208 offset:0xe00
	v_cvt_pk_bf16_f32 v130, v140, v141
	v_mfma_f32_32x32x16_bf16 v[32:47], a[228:231], a[164:167], v[32:47]
	ds_read_b64_tr_b16 v[172:173], v208 offset:0x1000
	v_exp_f32_e32 v234, v94
	v_exp_f32_e32 v235, v95
	ds_read_b64_tr_b16 v[174:175], v208 offset:0x1800
	v_cvt_pk_bf16_f32 v131, v142, v143
	v_exp_f32_e32 v141, v64
	v_exp_f32_e32 v142, v65
	v_mfma_f32_32x32x16_bf16 v[112:127], a[200:203], a[136:139], v[112:127]
	ds_read_b64_tr_b16 v[168:169], v208 offset:0x1200
	v_cvt_pk_bf16_f32 v192, v144, v145
	v_exp_f32_e32 v143, v66
	v_mfma_f32_32x32x16_bf16 v[96:111], a[200:203], a[168:171], v[96:111]
	ds_read_b64_tr_b16 v[170:171], v208 offset:0x1a00
	v_exp_f32_e32 v244, v67
	v_cvt_pk_bf16_f32 v193, v146, v147
	v_mfma_f32_32x32x16_bf16 v[48:63], a[232:235], a[136:139], v[48:63]
	ds_read_b64_tr_b16 v[160:161], v208 offset:0x1400
	v_exp_f32_e32 v245, v68
	v_exp_f32_e32 v246, v69
	v_cvt_pk_bf16_f32 v194, v148, v149
	v_mfma_f32_32x32x16_bf16 v[32:47], a[232:235], a[168:171], v[32:47]
	ds_read_b64_tr_b16 v[162:163], v208 offset:0x1c00
	ds_read_b64_tr_b16 v[136:137], v208 offset:0x1600
	v_exp_f32_e32 v247, v70
	v_exp_f32_e32 v248, v71
	v_cvt_pk_bf16_f32 v195, v150, v151
	v_exp_f32_e32 v148, v72
	v_exp_f32_e32 v149, v73
	v_mfma_f32_32x32x16_bf16 v[112:127], a[204:207], a[140:143], v[112:127]
	ds_read_b64_tr_b16 v[138:139], v208 offset:0x1e00
	v_cvt_pk_bf16_f32 v144, v152, v153
	v_exp_f32_e32 v150, v74
	v_exp_f32_e32 v151, v75
	v_mfma_f32_32x32x16_bf16 v[96:111], a[204:207], a[172:175], v[96:111]
	ds_read_b64_tr_b16 v[132:133], v208 offset:0x2000
	v_cvt_pk_bf16_f32 v145, v154, v155
	v_exp_f32_e32 v152, v76
	v_exp_f32_e32 v153, v77
	v_mfma_f32_32x32x16_bf16 v[48:63], a[236:239], a[140:143], v[48:63]
	ds_read_b64_tr_b16 v[134:135], v208 offset:0x2800
	v_cvt_pk_bf16_f32 v146, v156, v157
	v_mfma_f32_32x32x16_bf16 v[32:47], a[236:239], a[172:175], v[32:47]
	ds_read_b64_tr_b16 v[92:93], v208 offset:0x2200
	v_exp_f32_e32 v154, v78
	v_exp_f32_e32 v155, v79
	ds_read_b64_tr_b16 v[94:95], v208 offset:0x2a00
	v_cvt_pk_bf16_f32 v147, v158, v159
	v_mfma_f32_32x32x16_bf16 v[112:127], a[208:211], a[144:147], v[112:127]
	ds_read_b64_tr_b16 v[88:89], v208 offset:0x2400
	v_cvt_pk_bf16_f32 v84, v80, v81
	v_add_f32_e32 v64, v237, v80
	v_add_f32_e32 v65, v236, v81
	s_add_i32 s1, s17, 0xffffa000
	v_mfma_f32_32x32x16_bf16 v[96:111], a[208:211], a[176:179], v[96:111]
	ds_read_b64_tr_b16 v[90:91], v208 offset:0x2c00
	v_cvt_pk_bf16_f32 v85, v82, v83
	v_add_f32_e32 v64, v64, v82
	v_add_f32_e32 v65, v65, v83
	v_mfma_f32_32x32x16_bf16 v[48:63], a[240:243], a[144:147], v[48:63]
	ds_read_b64_tr_b16 v[80:81], v208 offset:0x2600
	v_cvt_pk_bf16_f32 v86, v240, v241
	v_add_f32_e32 v64, v64, v240
	v_add_f32_e32 v65, v65, v241
	s_add_i32 s82, s17, 0xffffc000
	v_mfma_f32_32x32x16_bf16 v[32:47], a[240:243], a[176:179], v[32:47]
	ds_read_b64_tr_b16 v[82:83], v208 offset:0x2e00
	ds_read_b64_tr_b16 v[76:77], v208 offset:0x3000
	v_cvt_pk_bf16_f32 v87, v242, v243
	v_add_f32_e32 v64, v64, v242
	v_add_f32_e32 v65, v65, v243
	v_mfma_f32_32x32x16_bf16 v[112:127], a[212:215], a[148:151], v[112:127]
	ds_read_b64_tr_b16 v[78:79], v208 offset:0x3800
	v_add_f32_e32 v64, v64, v198
	v_add_f32_e32 v65, v65, v199
	s_add_i32 s84, s17, 0xffffe000
	v_mfma_f32_32x32x16_bf16 v[96:111], a[212:215], a[180:183], v[96:111]
	ds_read_b64_tr_b16 v[72:73], v208 offset:0x3200
	v_add_f32_e32 v64, v64, v230
	v_add_f32_e32 v65, v65, v231
	v_mfma_f32_32x32x16_bf16 v[48:63], a[244:247], a[148:151], v[48:63]
	ds_read_b64_tr_b16 v[74:75], v208 offset:0x3a00
	v_add_f32_e32 v64, v64, v232
	v_add_f32_e32 v65, v65, v233
	v_mfma_f32_32x32x16_bf16 v[32:47], a[244:247], a[180:183], v[32:47]
	ds_read_b64_tr_b16 v[68:69], v208 offset:0x3400
	ds_read_b64_tr_b16 v[70:71], v208 offset:0x3c00
	v_add_f32_e32 v156, v64, v234
	v_add_f32_e32 v157, v65, v235
	v_mfma_f32_32x32x16_bf16 v[112:127], a[216:219], a[152:155], v[112:127]
	ds_read_b64_tr_b16 v[64:65], v208 offset:0x3600
	v_cvt_pk_bf16_f32 v140, v141, v142
	v_add_f32_e32 v158, v238, v141
	v_add_f32_e32 v142, v239, v142
	v_mfma_f32_32x32x16_bf16 v[96:111], a[216:219], a[184:187], v[96:111]
	ds_read_b64_tr_b16 v[66:67], v208 offset:0x3e00
	v_cvt_pk_bf16_f32 v141, v143, v244
	v_add_f32_e32 v143, v158, v143
	v_add_f32_e32 v158, v142, v244
	v_mfma_f32_32x32x16_bf16 v[48:63], a[248:251], a[152:155], v[48:63]
	v_cvt_pk_bf16_f32 v142, v245, v246
	v_add_f32_e32 v159, v143, v245
	v_add_f32_e32 v158, v158, v246
	v_mfma_f32_32x32x16_bf16 v[32:47], a[248:251], a[184:187], v[32:47]
	s_add_i32 s89, s17, 0xfffda080
	v_cvt_pk_bf16_f32 v143, v247, v248
	v_add_f32_e32 v159, v159, v247
	v_add_f32_e32 v158, v158, v248
	v_mfma_f32_32x32x16_bf16 v[112:127], a[220:223], a[156:159], v[112:127]
	v_add_f32_e32 v159, v159, v148
	v_add_f32_e32 v158, v158, v149
	v_mfma_f32_32x32x16_bf16 v[96:111], a[220:223], a[188:191], v[96:111]
	v_add_f32_e32 v159, v159, v150
	v_add_f32_e32 v158, v158, v151
	v_mfma_f32_32x32x16_bf16 v[48:63], a[252:255], a[156:159], v[48:63]
	v_add_f32_e32 v159, v159, v152
	v_add_f32_e32 v158, v158, v153
	v_mfma_f32_32x32x16_bf16 v[32:47], a[252:255], a[188:191], v[32:47]
	s_add_i32 s92, s17, 0xfffde080
	v_add_f32_e32 v159, v159, v154
	v_add_f32_e32 v158, v158, v155
	s_nop 4
	v_add_f32_e32 v156, v156, v157
	s_waitcnt vmcnt(0) lgkmcnt(0)
	s_barrier
	s_nop 0
	v_mov_b32_e32 v157, v156
	s_nop 1
	v_permlane32_swap_b32_e32 v156, v157
	v_add_f32_e32 v156, v156, v157
	v_add_f32_e32 v197, v197, v156
	v_add_f32_e32 v156, v159, v158
	v_mov_b32_e32 v157, v156
	s_nop 1
	v_permlane32_swap_b32_e32 v156, v157
	v_add_f32_e32 v156, v156, v157
	v_add_f32_e32 v196, v196, v156
	s_nop 1
	v_mfma_f32_32x32x16_bf16 a[0:15], v[180:183], v[164:167], a[0:15]
	s_mov_b32 m0, s51
	s_nop 0
	buffer_load_dwordx4 v209, s[4:7], s1 offen lds
	v_mfma_f32_32x32x16_bf16 a[16:31], v[180:183], v[192:195], a[16:31]
	s_mov_b32 m0, s53
	s_nop 0
	buffer_load_dwordx4 v210, s[4:7], s82 offen lds
	ds_read_b128 a[192:195], v204 offset:0
	v_mfma_f32_32x32x16_bf16 a[32:47], v[184:187], v[164:167], a[32:47]
	s_mov_b32 m0, s55
	s_nop 0
	buffer_load_dwordx4 v209, s[4:7], s84 offen lds
	ds_read_b128 a[196:199], v205 offset:0
	v_mfma_f32_32x32x16_bf16 a[48:63], v[184:187], v[192:195], a[48:63]
	s_mov_b32 m0, s57
	s_nop 0
	buffer_load_dwordx4 v210, s[4:7], s17 offen lds
	ds_read_b128 a[200:203], v206 offset:0
	v_mfma_f32_32x32x16_bf16 a[64:79], v[176:179], v[164:167], a[64:79]
	s_mov_b32 m0, s31
	s_nop 0
	buffer_load_dwordx4 v211, s[20:23], s19 offen lds
	ds_read_b128 a[204:207], v207 offset:0
	v_mfma_f32_32x32x16_bf16 a[80:95], v[176:179], v[192:195], a[80:95]
	s_mov_b32 m0, s59
	s_nop 0
	buffer_load_dwordx4 v211, s[20:23], s89 offen lds
	ds_read_b128 a[208:211], v204 offset:128
	v_mfma_f32_32x32x16_bf16 a[96:111], v[188:191], v[164:167], a[96:111]
	s_mov_b32 m0, s61
	s_nop 0
	buffer_load_dwordx4 v211, s[20:23], s24 offen lds
	ds_read_b128 a[212:215], v205 offset:128
	v_mfma_f32_32x32x16_bf16 a[112:127], v[188:191], v[192:195], a[112:127]
	s_mov_b32 m0, s62
	s_nop 0
	buffer_load_dwordx4 v211, s[20:23], s92 offen lds
	ds_read_b128 a[216:219], v206 offset:128
	v_mfma_f32_32x32x16_bf16 a[0:15], v[172:175], v[128:131], a[0:15]
	ds_read_b128 a[220:223], v207 offset:128
	v_max3_f32 v156, v112, v113, v48
	v_max3_f32 v157, v114, v115, v49
	v_max3_f32 v156, v156, v50, v51
	v_mfma_f32_32x32x16_bf16 a[16:31], v[172:175], v[144:147], a[16:31]
	ds_read_b128 a[224:227], v204 offset:8192
	v_max3_f32 v156, v156, v116, v117
	v_max3_f32 v157, v157, v118, v119
	v_max3_f32 v156, v156, v52, v53
	v_max3_f32 v157, v157, v54, v55
	v_mfma_f32_32x32x16_bf16 a[32:47], v[168:171], v[128:131], a[32:47]
	ds_read_b128 a[228:231], v205 offset:8192
	v_max3_f32 v156, v156, v120, v121
	v_max3_f32 v157, v157, v122, v123
	v_max3_f32 v156, v156, v56, v57
	v_max3_f32 v157, v157, v58, v59
	v_mfma_f32_32x32x16_bf16 a[48:63], v[168:171], v[144:147], a[48:63]
	ds_read_b128 a[232:235], v206 offset:8192
	v_max3_f32 v156, v156, v124, v125
	v_max3_f32 v157, v157, v126, v127
	v_max3_f32 v156, v156, v60, v61
	v_max3_f32 v157, v157, v62, v63
	v_mfma_f32_32x32x16_bf16 a[64:79], v[160:163], v[128:131], a[64:79]
	ds_read_b128 a[236:239], v207 offset:8192
	v_max3_f32 v158, v96, v97, v32
	v_max3_f32 v159, v98, v99, v33
	v_max3_f32 v158, v158, v34, v35
	v_mfma_f32_32x32x16_bf16 a[80:95], v[160:163], v[144:147], a[80:95]
	ds_read_b128 a[240:243], v204 offset:8320
	v_max3_f32 v158, v158, v100, v101
	v_max3_f32 v159, v159, v102, v103
	v_max3_f32 v158, v158, v36, v37
	v_max3_f32 v159, v159, v38, v39
	v_mfma_f32_32x32x16_bf16 a[96:111], v[136:139], v[128:131], a[96:111]
	ds_read_b128 a[244:247], v205 offset:8320
	v_max3_f32 v128, v158, v104, v105
	v_max3_f32 v129, v159, v106, v107
	v_max3_f32 v128, v128, v40, v41
	v_max3_f32 v129, v129, v42, v43
	v_mfma_f32_32x32x16_bf16 a[112:127], v[136:139], v[144:147], a[112:127]
	ds_read_b128 a[248:251], v206 offset:8320
	v_max3_f32 v128, v128, v108, v109
	v_max3_f32 v129, v129, v110, v111
	v_max3_f32 v128, v128, v44, v45
	v_max3_f32 v130, v129, v46, v47
	v_mfma_f32_32x32x16_bf16 a[0:15], v[132:135], v[84:87], a[0:15]
	ds_read_b128 a[252:255], v207 offset:8320
	v_max_f32_e32 v129, v156, v157
	v_mov_b32_e32 v131, v129
	s_nop 1
	v_permlane32_swap_b32_e32 v129, v131
	v_max_f32_e32 v129, v129, v131
	v_mfma_f32_32x32x16_bf16 a[16:31], v[132:135], v[140:143], a[16:31]
	v_max_f32_e32 v128, v128, v130
	v_mov_b32_e32 v130, v128
	s_nop 1
	v_permlane32_swap_b32_e32 v128, v130
	v_max_f32_e32 v128, v128, v130
	v_max_f32_e32 v130, v129, v129
	v_max_f32_e32 v131, v128, v128
	v_max_f32_e32 v130, v130, v131
	v_mfma_f32_32x32x16_bf16 a[32:47], v[92:95], v[84:87], a[32:47]
	v_cmp_lt_f32_e32 vcc, s79, v130
	s_cmp_lg_u64 vcc, 0
	s_cselect_b64 s[0:1], -1, 0
	s_cbranch_vccnz .LBB2_20
